# phase 0 gate finalize: the 8 bias loads requested together up front instead of one load behind every store (8 serialised round trips of a single wave removed)
# speedup vs baseline: 1.0018x; 1.0018x over previous
; template <int MODE, bool OUTF32, bool HIN16 = false, bool HOUT16 = false>
; __device__ __forceinline__ void row_phase(LAS unsigned char* lds, const RowArgs& a, int G) {
;     ...
;         if (tid < 32) {
;             const int r = tid, row = row0 + r;
;             float s = 0.f;
; #pragma unroll
;             for (int w = 0; w < 8; ++w) s += red[(r * 8 + w) * NRED + 36];
;             const float rstd = rsqrtf(s * (1.0f / D) + EPS);
;             rstd_l[r] = rstd; frs = rstd;
;             if constexpr (MODE == RM_GATES) {
; #pragma unroll
;                 for (int o = 0; o < 8; ++o) { float d = 0.f;
; #pragma unroll
;                     for (int w = 0; w < 8; ++w) d += red[(r * 8 + w) * NRED + o];
;                     a.gates[(size_t)row * 8 + o] = d * rstd + a.bgate[o]; }
.LBB0_162:
	s_or_b64 exec, exec, s[14:15]
	s_waitcnt lgkmcnt(0)
	s_barrier
	s_and_saveexec_b64 s[26:27], s[10:11]
	s_cbranch_execz .LBB0_33
	global_load_dwordx4 v[226:229], v155, s[22:23]
	global_load_dwordx4 v[230:233], v155, s[22:23] offset:16
	ds_read2_b32 v[158:159], v154 offset0:36 offset1:76
	ds_read2_b32 v[160:161], v154 offset0:116 offset1:156
	v_add_u32_e32 v162, 0x400, v154
	ds_read2_b32 v[162:163], v162 offset0:20 offset1:60
	s_waitcnt lgkmcnt(2)
	v_add_f32_e32 v158, 0, v158
	v_add_f32_e32 v164, v158, v159
	ds_read2_b32 v[158:159], v154 offset0:196 offset1:236
	s_waitcnt lgkmcnt(2)
	v_add_f32_e32 v160, v164, v160
	v_add_f32_e32 v160, v160, v161
	s_waitcnt lgkmcnt(0)
	v_add_f32_e32 v158, v160, v158
	v_add_f32_e32 v158, v158, v159
	v_add_f32_e32 v158, v158, v162
	v_add_f32_e32 v158, v158, v163
	v_fmamk_f32 v158, v158, 0x3a000000, v156
	v_mul_f32_e32 v159, 0x4b800000, v158
	v_cmp_gt_f32_e64 s[14:15], s54, v158
	s_nop 1
	v_cndmask_b32_e64 v158, v158, v159, s[14:15]
	v_rsq_f32_e32 v159, v158
	v_add_u32_e32 v158, s20, v1
	v_subrev_u32_e32 v158, 31, v158
	v_mul_f32_e32 v160, 0x45800000, v159
	v_cndmask_b32_e64 v225, v159, v160, s[14:15]
	ds_write_b32 v152, v225 offset:40960
	ds_read2_b32 v[160:161], v154 offset1:1
	ds_read2_b32 v[162:163], v154 offset0:2 offset1:3
	ds_read2_b32 v[164:165], v154 offset0:4 offset1:5
	ds_read2_b32 v[166:167], v154 offset0:6 offset1:7
	ds_read2_b32 v[168:169], v154 offset0:40 offset1:41
	ds_read2_b32 v[170:171], v154 offset0:80 offset1:81
	ds_read2_b32 v[172:173], v154 offset0:42 offset1:43
	ds_read2_b32 v[174:175], v154 offset0:44 offset1:45
	ds_read2_b32 v[176:177], v154 offset0:46 offset1:47
	ds_read2_b32 v[178:179], v154 offset0:82 offset1:83
	ds_read2_b32 v[180:181], v154 offset0:84 offset1:85
	ds_read2_b32 v[182:183], v154 offset0:86 offset1:87
	ds_read2_b32 v[184:185], v154 offset0:120 offset1:121
	ds_read2_b32 v[186:187], v154 offset0:160 offset1:161
	ds_read2_b32 v[188:189], v154 offset0:122 offset1:123
	ds_read2_b32 v[190:191], v154 offset0:124 offset1:125
	ds_read2_b32 v[192:193], v154 offset0:126 offset1:127
	s_waitcnt lgkmcnt(14)
	v_add_f32_e32 v160, 0, v160
	s_waitcnt lgkmcnt(12)
	v_add_f32_e32 v160, v160, v168
	v_add_u32_e32 v168, 0x460, v154
	s_waitcnt lgkmcnt(11)
	v_add_f32_e32 v160, v160, v170
	ds_read2_b32 v[194:195], v154 offset0:162 offset1:163
	ds_read2_b32 v[196:197], v154 offset0:164 offset1:165
	ds_read2_b32 v[198:199], v154 offset0:166 offset1:167
	ds_read2_b32 v[200:201], v154 offset0:200 offset1:201
	ds_read2_b32 v[202:203], v154 offset0:240 offset1:241
	ds_read2_b32 v[204:205], v154 offset0:202 offset1:203
	ds_read2_b32 v[206:207], v154 offset0:204 offset1:205
	ds_read2_b32 v[208:209], v154 offset0:206 offset1:207
	ds_read2_b32 v[210:211], v154 offset0:242 offset1:243
	ds_read2_b32 v[212:213], v154 offset0:244 offset1:245
	ds_read2_b32 v[214:215], v154 offset0:246 offset1:247
	ds_read2_b32 v[216:217], v168 offset1:1
	s_waitcnt lgkmcnt(14)
	v_add_f32_e32 v160, v160, v184
	v_add_f32_e32 v160, v160, v186
	s_waitcnt lgkmcnt(8)
	v_add_f32_e32 v160, v160, v200
	v_ashrrev_i32_e32 v159, 31, v158
	s_waitcnt lgkmcnt(7)
	v_add_f32_e32 v160, v160, v202
	v_lshlrev_b64 v[158:159], 5, v[158:159]
	s_waitcnt lgkmcnt(0)
	v_add_f32_e32 v160, v160, v216
	v_lshl_add_u64 v[158:159], s[24:25], 0, v[158:159]
	v_add_u32_e32 v168, 0x468, v154
	v_add_u32_e32 v170, 0x470, v154
	v_add_u32_e32 v184, 0x478, v154
	ds_read2_b32 v[218:219], v168 offset1:1
	ds_read2_b32 v[220:221], v170 offset1:1
	ds_read2_b32 v[222:223], v184 offset1:1
	v_add_f32_e32 v161, 0, v161
	v_add_f32_e32 v161, v161, v169
	v_add_f32_e32 v161, v161, v171
	v_add_f32_e32 v161, v161, v185
	v_add_f32_e32 v161, v161, v187
	v_add_f32_e32 v161, v161, v201
	v_add_f32_e32 v161, v161, v203
	v_add_f32_e32 v161, v161, v217
	s_waitcnt vmcnt(0)
	v_fmac_f32_e32 v226, v225, v160
	global_store_dword v[158:159], v226, off
	v_fmac_f32_e32 v227, v225, v161
	global_store_dword v[158:159], v227, off offset:4
	v_add_f32_e32 v161, 0, v162
	v_add_f32_e32 v161, v161, v172
	v_add_f32_e32 v161, v161, v178
	v_add_f32_e32 v161, v161, v188
	v_add_f32_e32 v161, v161, v194
	v_add_f32_e32 v161, v161, v204
	v_add_f32_e32 v161, v161, v210
	s_waitcnt lgkmcnt(2)
	v_add_f32_e32 v161, v161, v218
	v_fmac_f32_e32 v228, v225, v161
	global_store_dword v[158:159], v228, off offset:8
	v_add_f32_e32 v161, 0, v163
	v_add_f32_e32 v161, v161, v173
	v_add_f32_e32 v161, v161, v179
	v_add_f32_e32 v161, v161, v189
	v_add_f32_e32 v161, v161, v195
	v_add_f32_e32 v161, v161, v205
	v_add_f32_e32 v161, v161, v211
	v_add_f32_e32 v161, v161, v219
	v_fmac_f32_e32 v229, v225, v161
	global_store_dword v[158:159], v229, off offset:12
	v_add_f32_e32 v161, 0, v164
	v_add_f32_e32 v161, v161, v174
	v_add_f32_e32 v161, v161, v180
	v_add_f32_e32 v161, v161, v190
	v_add_f32_e32 v161, v161, v196
	v_add_f32_e32 v161, v161, v206
	v_add_f32_e32 v161, v161, v212
	s_waitcnt lgkmcnt(1)
	v_add_f32_e32 v161, v161, v220
	v_fmac_f32_e32 v230, v225, v161
	global_store_dword v[158:159], v230, off offset:16
	v_add_f32_e32 v161, 0, v165
	v_add_f32_e32 v161, v161, v175
	v_add_f32_e32 v161, v161, v181
	v_add_f32_e32 v161, v161, v191
	v_add_f32_e32 v161, v161, v197
	v_add_f32_e32 v161, v161, v207
	v_add_f32_e32 v161, v161, v213
	v_add_f32_e32 v161, v161, v221
	v_fmac_f32_e32 v231, v225, v161
	global_store_dword v[158:159], v231, off offset:20
	v_add_f32_e32 v161, 0, v166
	v_add_f32_e32 v161, v161, v176
	v_add_f32_e32 v161, v161, v182
	v_add_f32_e32 v161, v161, v192
	v_add_f32_e32 v161, v161, v198
	v_add_f32_e32 v161, v161, v208
	v_add_f32_e32 v161, v161, v214
	s_waitcnt lgkmcnt(0)
	v_add_f32_e32 v161, v161, v222
	v_fmac_f32_e32 v232, v225, v161
	global_store_dword v[158:159], v232, off offset:24
	v_add_f32_e32 v161, 0, v167
	v_add_f32_e32 v161, v161, v177
	v_add_f32_e32 v161, v161, v183
	v_add_f32_e32 v161, v161, v193
	v_add_f32_e32 v161, v161, v199
	v_add_f32_e32 v161, v161, v209
	v_add_f32_e32 v161, v161, v215
	v_add_f32_e32 v161, v161, v223
	v_fmac_f32_e32 v233, v225, v161
	global_store_dword v[158:159], v233, off offset:28
	s_branch .LBB0_33
